# baseline (speedup 1.0000x reference)
.LBB1_65:
	s_or_b64 exec, exec, s[2:3]
	v_add_u32_e32 v67, v222, v224
	ds_read2st64_b32 v[76:77], v223 offset1:2
	s_cmp_eq_u64 s[6:7], 0
	s_cbranch_scc0 .Lep1_pre1
	ds_read2st64_b32 v[62:63], v67 offset0:0 offset1:2
	ds_read2st64_b32 v[64:65], v67 offset0:4 offset1:6
	ds_read2st64_b32 v[68:69], v67 offset0:16 offset1:18
	ds_read2st64_b32 v[70:71], v67 offset0:20 offset1:22
	ds_read2st64_b32 v[72:73], v67 offset0:32 offset1:34
	ds_read2st64_b32 v[74:75], v67 offset0:36 offset1:38
	s_branch .Lep1_prej
.Lep1_pre1:
	ds_read2st64_b32 v[62:63], v67 offset0:96 offset1:98
	ds_read2st64_b32 v[64:65], v67 offset0:100 offset1:102
	ds_read2st64_b32 v[68:69], v67 offset0:112 offset1:114
	ds_read2st64_b32 v[70:71], v67 offset0:116 offset1:118
	ds_read2st64_b32 v[72:73], v67 offset0:128 offset1:130
	ds_read2st64_b32 v[74:75], v67 offset0:132 offset1:134
.Lep1_prej:
	s_waitcnt lgkmcnt(7)
	s_barrier
	s_cmp_eq_u64 s[6:7], 0
	s_cbranch_scc0 .Lep1_k1
	v_mov_b32_e32 v18, 0
	v_mov_b32_e32 v19, 0
	v_mov_b32_e32 v20, 0
	v_mov_b32_e32 v21, 0
	ds_read2st64_b32 v[50:51], v221 offset0:0 offset1:1
	ds_read2st64_b32 v[52:53], v221 offset0:2 offset1:3
	ds_read2st64_b32 v[54:55], v221 offset0:4 offset1:5
	ds_read2st64_b32 v[56:57], v221 offset0:6 offset1:7
	ds_read2st64_b32 v[58:59], v221 offset0:8 offset1:9
	ds_read2st64_b32 v[60:61], v221 offset0:10 offset1:11
	s_waitcnt lgkmcnt(12)
	v_fma_f32 v78, -v76, v77, 0
	s_waitcnt lgkmcnt(4)
	v_pk_add_f32 v[34:35], v[34:35], v[50:51]
	v_pk_add_f32 v[36:37], v[36:37], v[52:53]
	v_pk_add_f32 v[34:35], v[34:35], v[78:79] op_sel_hi:[1,0]
	v_pk_add_f32 v[36:37], v[36:37], v[78:79] op_sel_hi:[1,0]
	v_pk_fma_f32 v[34:35], v[62:63], v[76:77], v[34:35] op_sel:[0,1,0] op_sel_hi:[1,1,1]
	v_pk_fma_f32 v[36:37], v[64:65], v[76:77], v[36:37] op_sel:[0,1,0] op_sel_hi:[1,1,1]
	v_pk_add_f32 v[18:19], v[18:19], v[34:35]
	v_pk_fma_f32 v[20:21], v[34:35], v[34:35], v[20:21]
	v_pk_add_f32 v[18:19], v[18:19], v[36:37]
	v_pk_fma_f32 v[20:21], v[36:37], v[36:37], v[20:21]
	s_waitcnt lgkmcnt(2)
	v_pk_add_f32 v[38:39], v[38:39], v[54:55]
	v_pk_add_f32 v[40:41], v[40:41], v[56:57]
	v_pk_add_f32 v[38:39], v[38:39], v[78:79] op_sel_hi:[1,0]
	v_pk_add_f32 v[40:41], v[40:41], v[78:79] op_sel_hi:[1,0]
	v_pk_fma_f32 v[38:39], v[68:69], v[76:77], v[38:39] op_sel:[0,1,0] op_sel_hi:[1,1,1]
	v_pk_fma_f32 v[40:41], v[70:71], v[76:77], v[40:41] op_sel:[0,1,0] op_sel_hi:[1,1,1]
	v_pk_add_f32 v[18:19], v[18:19], v[38:39]
	v_pk_fma_f32 v[20:21], v[38:39], v[38:39], v[20:21]
	v_pk_add_f32 v[18:19], v[18:19], v[40:41]
	v_pk_fma_f32 v[20:21], v[40:41], v[40:41], v[20:21]
	s_waitcnt lgkmcnt(0)
	v_pk_add_f32 v[42:43], v[42:43], v[58:59]
	v_pk_add_f32 v[44:45], v[44:45], v[60:61]
	v_pk_add_f32 v[42:43], v[42:43], v[78:79] op_sel_hi:[1,0]
	v_pk_add_f32 v[44:45], v[44:45], v[78:79] op_sel_hi:[1,0]
	v_pk_fma_f32 v[42:43], v[72:73], v[76:77], v[42:43] op_sel:[0,1,0] op_sel_hi:[1,1,1]
	v_pk_fma_f32 v[44:45], v[74:75], v[76:77], v[44:45] op_sel:[0,1,0] op_sel_hi:[1,1,1]
	v_pk_add_f32 v[18:19], v[18:19], v[42:43]
	v_pk_fma_f32 v[20:21], v[42:43], v[42:43], v[20:21]
	v_pk_add_f32 v[18:19], v[18:19], v[44:45]
	v_pk_fma_f32 v[20:21], v[44:45], v[44:45], v[20:21]
	ds_read2st64_b32 v[50:51], v221 offset0:12 offset1:13
	ds_read2st64_b32 v[52:53], v221 offset0:14 offset1:15
	ds_read2st64_b32 v[54:55], v221 offset0:16 offset1:17
	ds_read2st64_b32 v[56:57], v221 offset0:18 offset1:19
	ds_read2st64_b32 v[58:59], v221 offset0:20 offset1:21
	ds_read2st64_b32 v[60:61], v221 offset0:22 offset1:23
	ds_read2st64_b32 v[62:63], v67 offset0:48 offset1:50
	ds_read2st64_b32 v[64:65], v67 offset0:52 offset1:54
	ds_read2st64_b32 v[68:69], v67 offset0:64 offset1:66
	ds_read2st64_b32 v[70:71], v67 offset0:68 offset1:70
	ds_read2st64_b32 v[72:73], v67 offset0:80 offset1:82
	ds_read2st64_b32 v[74:75], v67 offset0:84 offset1:86
	s_barrier
	ds_read_b32 v80, v236
	s_waitcnt lgkmcnt(5)
	v_pk_add_f32 v[46:47], v[46:47], v[50:51]
	v_pk_add_f32 v[48:49], v[48:49], v[52:53]
	v_pk_add_f32 v[46:47], v[46:47], v[78:79] op_sel_hi:[1,0]
	v_pk_add_f32 v[48:49], v[48:49], v[78:79] op_sel_hi:[1,0]
	v_pk_fma_f32 v[46:47], v[62:63], v[76:77], v[46:47] op_sel:[0,1,0] op_sel_hi:[1,1,1]
	v_pk_fma_f32 v[48:49], v[64:65], v[76:77], v[48:49] op_sel:[0,1,0] op_sel_hi:[1,1,1]
	v_pk_add_f32 v[18:19], v[18:19], v[46:47]
	v_pk_fma_f32 v[20:21], v[46:47], v[46:47], v[20:21]
	v_pk_add_f32 v[18:19], v[18:19], v[48:49]
	v_pk_fma_f32 v[20:21], v[48:49], v[48:49], v[20:21]
	s_waitcnt lgkmcnt(3)
	v_pk_add_f32 v[2:3], v[2:3], v[54:55]
	v_pk_add_f32 v[4:5], v[4:5], v[56:57]
	v_pk_add_f32 v[2:3], v[2:3], v[78:79] op_sel_hi:[1,0]
	v_pk_add_f32 v[4:5], v[4:5], v[78:79] op_sel_hi:[1,0]
	v_pk_fma_f32 v[2:3], v[68:69], v[76:77], v[2:3] op_sel:[0,1,0] op_sel_hi:[1,1,1]
	v_pk_fma_f32 v[4:5], v[70:71], v[76:77], v[4:5] op_sel:[0,1,0] op_sel_hi:[1,1,1]
	v_pk_add_f32 v[18:19], v[18:19], v[2:3]
	v_pk_fma_f32 v[20:21], v[2:3], v[2:3], v[20:21]
	v_pk_add_f32 v[18:19], v[18:19], v[4:5]
	v_pk_fma_f32 v[20:21], v[4:5], v[4:5], v[20:21]
	s_waitcnt lgkmcnt(1)
	v_pk_add_f32 v[6:7], v[6:7], v[58:59]
	v_pk_add_f32 v[8:9], v[8:9], v[60:61]
	v_pk_add_f32 v[6:7], v[6:7], v[78:79] op_sel_hi:[1,0]
	v_pk_add_f32 v[8:9], v[8:9], v[78:79] op_sel_hi:[1,0]
	v_pk_fma_f32 v[6:7], v[72:73], v[76:77], v[6:7] op_sel:[0,1,0] op_sel_hi:[1,1,1]
	v_pk_fma_f32 v[8:9], v[74:75], v[76:77], v[8:9] op_sel:[0,1,0] op_sel_hi:[1,1,1]
	v_pk_add_f32 v[18:19], v[18:19], v[6:7]
	v_pk_fma_f32 v[20:21], v[6:7], v[6:7], v[20:21]
	v_pk_add_f32 v[18:19], v[18:19], v[8:9]
	v_pk_fma_f32 v[20:21], v[8:9], v[8:9], v[20:21]
	v_add_f32_e32 v18, v18, v19
	v_add_f32_e32 v20, v20, v21
	v_mov_b32_e32 v19, v18
	v_mov_b32_e32 v21, v20
	s_nop 1
	v_permlane32_swap_b32_e32 v18, v19
	v_permlane32_swap_b32_e32 v20, v21
	v_add_f32_e32 v18, v18, v19
	v_add_f32_e32 v20, v20, v21
	v_cndmask_b32_e64 v22, v20, v18, s[0:1]
	s_branch .Lep1_wr0
.Lep1_k1:
	s_setprio 2
	v_mov_b32_e32 v34, 0
	v_mov_b32_e32 v35, 0
	v_mov_b32_e32 v36, 0
	v_mov_b32_e32 v37, 0
	ds_read2st64_b32 v[50:51], v221 offset0:24 offset1:25
	ds_read2st64_b32 v[52:53], v221 offset0:26 offset1:27
	ds_read2st64_b32 v[54:55], v221 offset0:28 offset1:29
	ds_read2st64_b32 v[56:57], v221 offset0:30 offset1:31
	ds_read2st64_b32 v[58:59], v221 offset0:32 offset1:33
	ds_read2st64_b32 v[60:61], v221 offset0:34 offset1:35
	s_waitcnt lgkmcnt(12)
	v_fma_f32 v78, -v76, v77, 0
	s_waitcnt lgkmcnt(4)
	v_pk_add_f32 v[10:11], v[10:11], v[50:51]
	v_pk_add_f32 v[12:13], v[12:13], v[52:53]
	v_pk_add_f32 v[10:11], v[10:11], v[78:79] op_sel_hi:[1,0]
	v_pk_add_f32 v[12:13], v[12:13], v[78:79] op_sel_hi:[1,0]
	v_pk_fma_f32 v[10:11], v[62:63], v[76:77], v[10:11] op_sel:[0,1,0] op_sel_hi:[1,1,1]
	v_pk_fma_f32 v[12:13], v[64:65], v[76:77], v[12:13] op_sel:[0,1,0] op_sel_hi:[1,1,1]
	v_pk_add_f32 v[34:35], v[34:35], v[10:11]
	v_pk_fma_f32 v[36:37], v[10:11], v[10:11], v[36:37]
	v_pk_add_f32 v[34:35], v[34:35], v[12:13]
	v_pk_fma_f32 v[36:37], v[12:13], v[12:13], v[36:37]
	s_waitcnt lgkmcnt(2)
	v_pk_add_f32 v[14:15], v[14:15], v[54:55]
	v_pk_add_f32 v[16:17], v[16:17], v[56:57]
	v_pk_add_f32 v[14:15], v[14:15], v[78:79] op_sel_hi:[1,0]
	v_pk_add_f32 v[16:17], v[16:17], v[78:79] op_sel_hi:[1,0]
	v_pk_fma_f32 v[14:15], v[68:69], v[76:77], v[14:15] op_sel:[0,1,0] op_sel_hi:[1,1,1]
	v_pk_fma_f32 v[16:17], v[70:71], v[76:77], v[16:17] op_sel:[0,1,0] op_sel_hi:[1,1,1]
	v_pk_add_f32 v[34:35], v[34:35], v[14:15]
	v_pk_fma_f32 v[36:37], v[14:15], v[14:15], v[36:37]
	v_pk_add_f32 v[34:35], v[34:35], v[16:17]
	v_pk_fma_f32 v[36:37], v[16:17], v[16:17], v[36:37]
	s_waitcnt lgkmcnt(0)
	v_pk_add_f32 v[18:19], v[18:19], v[58:59]
	v_pk_add_f32 v[20:21], v[20:21], v[60:61]
	v_pk_add_f32 v[18:19], v[18:19], v[78:79] op_sel_hi:[1,0]
	v_pk_add_f32 v[20:21], v[20:21], v[78:79] op_sel_hi:[1,0]
	v_pk_fma_f32 v[18:19], v[72:73], v[76:77], v[18:19] op_sel:[0,1,0] op_sel_hi:[1,1,1]
	v_pk_fma_f32 v[20:21], v[74:75], v[76:77], v[20:21] op_sel:[0,1,0] op_sel_hi:[1,1,1]
	v_pk_add_f32 v[34:35], v[34:35], v[18:19]
	v_pk_fma_f32 v[36:37], v[18:19], v[18:19], v[36:37]
	v_pk_add_f32 v[34:35], v[34:35], v[20:21]
	v_pk_fma_f32 v[36:37], v[20:21], v[20:21], v[36:37]
	ds_read2st64_b32 v[50:51], v221 offset0:36 offset1:37
	ds_read2st64_b32 v[52:53], v221 offset0:38 offset1:39
	ds_read2st64_b32 v[62:63], v67 offset0:144 offset1:146
	ds_read2st64_b32 v[64:65], v67 offset0:148 offset1:150
	s_waitcnt lgkmcnt(0)
	v_pk_add_f32 v[22:23], v[22:23], v[50:51]
	v_pk_add_f32 v[24:25], v[24:25], v[52:53]
	v_pk_add_f32 v[22:23], v[22:23], v[78:79] op_sel_hi:[1,0]
	v_pk_add_f32 v[24:25], v[24:25], v[78:79] op_sel_hi:[1,0]
	v_pk_fma_f32 v[22:23], v[62:63], v[76:77], v[22:23] op_sel:[0,1,0] op_sel_hi:[1,1,1]
	v_pk_fma_f32 v[24:25], v[64:65], v[76:77], v[24:25] op_sel:[0,1,0] op_sel_hi:[1,1,1]
	v_pk_add_f32 v[34:35], v[34:35], v[22:23]
	v_pk_fma_f32 v[36:37], v[22:23], v[22:23], v[36:37]
	v_pk_add_f32 v[34:35], v[34:35], v[24:25]
	v_pk_fma_f32 v[36:37], v[24:25], v[24:25], v[36:37]
	s_mov_b64 s[40:41], exec
	s_and_b64 exec, exec, s[0:1]
	ds_read2st64_b32 v[50:51], v221 offset0:40 offset1:41
	ds_read2st64_b32 v[52:53], v221 offset0:42 offset1:43
	ds_read2st64_b32 v[62:63], v67 offset0:160 offset1:162
	ds_read2st64_b32 v[64:65], v67 offset0:164 offset1:166
	s_waitcnt lgkmcnt(0)
	v_pk_add_f32 v[26:27], v[26:27], v[50:51]
	v_pk_add_f32 v[28:29], v[28:29], v[52:53]
	v_pk_add_f32 v[26:27], v[26:27], v[78:79] op_sel_hi:[1,0]
	v_pk_add_f32 v[28:29], v[28:29], v[78:79] op_sel_hi:[1,0]
	v_pk_fma_f32 v[26:27], v[62:63], v[76:77], v[26:27] op_sel:[0,1,0] op_sel_hi:[1,1,1]
	v_pk_fma_f32 v[28:29], v[64:65], v[76:77], v[28:29] op_sel:[0,1,0] op_sel_hi:[1,1,1]
	v_pk_add_f32 v[34:35], v[34:35], v[26:27]
	v_pk_fma_f32 v[36:37], v[26:27], v[26:27], v[36:37]
	v_pk_add_f32 v[34:35], v[34:35], v[28:29]
	v_pk_fma_f32 v[36:37], v[28:29], v[28:29], v[36:37]
	s_mov_b64 exec, s[40:41]
	v_add_f32_e32 v34, v34, v35
	v_add_f32_e32 v36, v36, v37
	v_mov_b32_e32 v35, v34
	v_mov_b32_e32 v37, v36
	s_nop 1
	v_permlane32_swap_b32_e32 v34, v35
	v_permlane32_swap_b32_e32 v36, v37
	v_add_f32_e32 v34, v34, v35
	v_add_f32_e32 v36, v36, v37
	v_cndmask_b32_e64 v38, v36, v34, s[0:1]
	ds_write_b32 v236, v38

.Lep2_prej:
	s_waitcnt lgkmcnt(7)
	s_barrier
	s_cmp_eq_u64 s[6:7], 0
	s_cbranch_scc0 .Lep2_k1
	v_mov_b32_e32 v18, 0
	v_mov_b32_e32 v19, 0
	v_mov_b32_e32 v20, 0
	v_mov_b32_e32 v21, 0
	ds_read2st64_b32 v[50:51], v221 offset0:0 offset1:1
	ds_read2st64_b32 v[52:53], v221 offset0:2 offset1:3
	ds_read2st64_b32 v[54:55], v221 offset0:4 offset1:5
	ds_read2st64_b32 v[56:57], v221 offset0:6 offset1:7
	ds_read2st64_b32 v[58:59], v221 offset0:8 offset1:9
	ds_read2st64_b32 v[60:61], v221 offset0:10 offset1:11
	s_waitcnt lgkmcnt(12)
	v_fma_f32 v78, -v76, v77, v173
	s_waitcnt lgkmcnt(4)
	v_pk_add_f32 v[34:35], v[34:35], v[50:51]
	v_pk_add_f32 v[36:37], v[36:37], v[52:53]
	v_pk_add_f32 v[34:35], v[34:35], v[78:79] op_sel_hi:[1,0]
	v_pk_add_f32 v[36:37], v[36:37], v[78:79] op_sel_hi:[1,0]
	v_pk_fma_f32 v[34:35], v[62:63], v[76:77], v[34:35] op_sel:[0,1,0] op_sel_hi:[1,1,1]
	v_pk_fma_f32 v[36:37], v[64:65], v[76:77], v[36:37] op_sel:[0,1,0] op_sel_hi:[1,1,1]
	v_pk_add_f32 v[18:19], v[18:19], v[34:35]
	v_pk_fma_f32 v[20:21], v[34:35], v[34:35], v[20:21]
	v_pk_add_f32 v[18:19], v[18:19], v[36:37]
	v_pk_fma_f32 v[20:21], v[36:37], v[36:37], v[20:21]
	s_waitcnt lgkmcnt(2)
	v_pk_add_f32 v[38:39], v[38:39], v[54:55]
	v_pk_add_f32 v[40:41], v[40:41], v[56:57]
	v_pk_add_f32 v[38:39], v[38:39], v[78:79] op_sel_hi:[1,0]
	v_pk_add_f32 v[40:41], v[40:41], v[78:79] op_sel_hi:[1,0]
	v_pk_fma_f32 v[38:39], v[68:69], v[76:77], v[38:39] op_sel:[0,1,0] op_sel_hi:[1,1,1]
	v_pk_fma_f32 v[40:41], v[70:71], v[76:77], v[40:41] op_sel:[0,1,0] op_sel_hi:[1,1,1]
	v_pk_add_f32 v[18:19], v[18:19], v[38:39]
	v_pk_fma_f32 v[20:21], v[38:39], v[38:39], v[20:21]
	v_pk_add_f32 v[18:19], v[18:19], v[40:41]
	v_pk_fma_f32 v[20:21], v[40:41], v[40:41], v[20:21]
	s_waitcnt lgkmcnt(0)
	v_pk_add_f32 v[42:43], v[42:43], v[58:59]
	v_pk_add_f32 v[44:45], v[44:45], v[60:61]
	v_pk_add_f32 v[42:43], v[42:43], v[78:79] op_sel_hi:[1,0]
	v_pk_add_f32 v[44:45], v[44:45], v[78:79] op_sel_hi:[1,0]
	v_pk_fma_f32 v[42:43], v[72:73], v[76:77], v[42:43] op_sel:[0,1,0] op_sel_hi:[1,1,1]
	v_pk_fma_f32 v[44:45], v[74:75], v[76:77], v[44:45] op_sel:[0,1,0] op_sel_hi:[1,1,1]
	v_pk_add_f32 v[18:19], v[18:19], v[42:43]
	v_pk_fma_f32 v[20:21], v[42:43], v[42:43], v[20:21]
	v_pk_add_f32 v[18:19], v[18:19], v[44:45]
	v_pk_fma_f32 v[20:21], v[44:45], v[44:45], v[20:21]
	ds_read2st64_b32 v[50:51], v221 offset0:12 offset1:13
	ds_read2st64_b32 v[52:53], v221 offset0:14 offset1:15
	ds_read2st64_b32 v[54:55], v221 offset0:16 offset1:17
	ds_read2st64_b32 v[56:57], v221 offset0:18 offset1:19
	ds_read2st64_b32 v[58:59], v221 offset0:20 offset1:21
	ds_read2st64_b32 v[60:61], v221 offset0:22 offset1:23
	ds_read2st64_b32 v[62:63], v67 offset0:48 offset1:50
	ds_read2st64_b32 v[64:65], v67 offset0:52 offset1:54
	ds_read2st64_b32 v[68:69], v67 offset0:64 offset1:66
	ds_read2st64_b32 v[70:71], v67 offset0:68 offset1:70
	ds_read2st64_b32 v[72:73], v67 offset0:80 offset1:82
	ds_read2st64_b32 v[74:75], v67 offset0:84 offset1:86
	s_barrier
	ds_read_b32 v80, v236
	s_waitcnt lgkmcnt(5)
	v_pk_add_f32 v[46:47], v[46:47], v[50:51]
	v_pk_add_f32 v[48:49], v[48:49], v[52:53]
	v_pk_add_f32 v[46:47], v[46:47], v[78:79] op_sel_hi:[1,0]
	v_pk_add_f32 v[48:49], v[48:49], v[78:79] op_sel_hi:[1,0]
	v_pk_fma_f32 v[46:47], v[62:63], v[76:77], v[46:47] op_sel:[0,1,0] op_sel_hi:[1,1,1]
	v_pk_fma_f32 v[48:49], v[64:65], v[76:77], v[48:49] op_sel:[0,1,0] op_sel_hi:[1,1,1]
	v_pk_add_f32 v[18:19], v[18:19], v[46:47]
	v_pk_fma_f32 v[20:21], v[46:47], v[46:47], v[20:21]
	v_pk_add_f32 v[18:19], v[18:19], v[48:49]
	v_pk_fma_f32 v[20:21], v[48:49], v[48:49], v[20:21]
	s_waitcnt lgkmcnt(3)
	v_pk_add_f32 v[2:3], v[2:3], v[54:55]
	v_pk_add_f32 v[4:5], v[4:5], v[56:57]
	v_pk_add_f32 v[2:3], v[2:3], v[78:79] op_sel_hi:[1,0]
	v_pk_add_f32 v[4:5], v[4:5], v[78:79] op_sel_hi:[1,0]
	v_pk_fma_f32 v[2:3], v[68:69], v[76:77], v[2:3] op_sel:[0,1,0] op_sel_hi:[1,1,1]
	v_pk_fma_f32 v[4:5], v[70:71], v[76:77], v[4:5] op_sel:[0,1,0] op_sel_hi:[1,1,1]
	v_pk_add_f32 v[18:19], v[18:19], v[2:3]
	v_pk_fma_f32 v[20:21], v[2:3], v[2:3], v[20:21]
	v_pk_add_f32 v[18:19], v[18:19], v[4:5]
	v_pk_fma_f32 v[20:21], v[4:5], v[4:5], v[20:21]
	s_waitcnt lgkmcnt(1)
	v_pk_add_f32 v[6:7], v[6:7], v[58:59]
	v_pk_add_f32 v[8:9], v[8:9], v[60:61]
	v_pk_add_f32 v[6:7], v[6:7], v[78:79] op_sel_hi:[1,0]
	v_pk_add_f32 v[8:9], v[8:9], v[78:79] op_sel_hi:[1,0]
	v_pk_fma_f32 v[6:7], v[72:73], v[76:77], v[6:7] op_sel:[0,1,0] op_sel_hi:[1,1,1]
	v_pk_fma_f32 v[8:9], v[74:75], v[76:77], v[8:9] op_sel:[0,1,0] op_sel_hi:[1,1,1]
	v_pk_add_f32 v[18:19], v[18:19], v[6:7]
	v_pk_fma_f32 v[20:21], v[6:7], v[6:7], v[20:21]
	v_pk_add_f32 v[18:19], v[18:19], v[8:9]
	v_pk_fma_f32 v[20:21], v[8:9], v[8:9], v[20:21]
	v_add_f32_e32 v18, v18, v19
	v_add_f32_e32 v20, v20, v21
	v_mov_b32_e32 v19, v18
	v_mov_b32_e32 v21, v20
	s_nop 1
	v_permlane32_swap_b32_e32 v18, v19
	v_permlane32_swap_b32_e32 v20, v21
	v_add_f32_e32 v18, v18, v19
	v_add_f32_e32 v20, v20, v21
	v_cndmask_b32_e64 v22, v20, v18, s[0:1]
	s_branch .Lep2_wr0
.Lep2_k1:
	s_setprio 2
	v_mov_b32_e32 v34, 0
	v_mov_b32_e32 v35, 0
	v_mov_b32_e32 v36, 0
	v_mov_b32_e32 v37, 0
	ds_read2st64_b32 v[50:51], v221 offset0:24 offset1:25
	ds_read2st64_b32 v[52:53], v221 offset0:26 offset1:27
	ds_read2st64_b32 v[54:55], v221 offset0:28 offset1:29
	ds_read2st64_b32 v[56:57], v221 offset0:30 offset1:31
	ds_read2st64_b32 v[58:59], v221 offset0:32 offset1:33
	ds_read2st64_b32 v[60:61], v221 offset0:34 offset1:35
	s_waitcnt lgkmcnt(12)
	v_fma_f32 v78, -v76, v77, v173
	s_waitcnt lgkmcnt(4)
	v_pk_add_f32 v[10:11], v[10:11], v[50:51]
	v_pk_add_f32 v[12:13], v[12:13], v[52:53]
	v_pk_add_f32 v[10:11], v[10:11], v[78:79] op_sel_hi:[1,0]
	v_pk_add_f32 v[12:13], v[12:13], v[78:79] op_sel_hi:[1,0]
	v_pk_fma_f32 v[10:11], v[62:63], v[76:77], v[10:11] op_sel:[0,1,0] op_sel_hi:[1,1,1]
	v_pk_fma_f32 v[12:13], v[64:65], v[76:77], v[12:13] op_sel:[0,1,0] op_sel_hi:[1,1,1]
	v_pk_add_f32 v[34:35], v[34:35], v[10:11]
	v_pk_fma_f32 v[36:37], v[10:11], v[10:11], v[36:37]
	v_pk_add_f32 v[34:35], v[34:35], v[12:13]
	v_pk_fma_f32 v[36:37], v[12:13], v[12:13], v[36:37]
	s_waitcnt lgkmcnt(2)
	v_pk_add_f32 v[14:15], v[14:15], v[54:55]
	v_pk_add_f32 v[16:17], v[16:17], v[56:57]
	v_pk_add_f32 v[14:15], v[14:15], v[78:79] op_sel_hi:[1,0]
	v_pk_add_f32 v[16:17], v[16:17], v[78:79] op_sel_hi:[1,0]
	v_pk_fma_f32 v[14:15], v[68:69], v[76:77], v[14:15] op_sel:[0,1,0] op_sel_hi:[1,1,1]
	v_pk_fma_f32 v[16:17], v[70:71], v[76:77], v[16:17] op_sel:[0,1,0] op_sel_hi:[1,1,1]
	v_pk_add_f32 v[34:35], v[34:35], v[14:15]
	v_pk_fma_f32 v[36:37], v[14:15], v[14:15], v[36:37]
	v_pk_add_f32 v[34:35], v[34:35], v[16:17]
	v_pk_fma_f32 v[36:37], v[16:17], v[16:17], v[36:37]
	s_waitcnt lgkmcnt(0)
	v_pk_add_f32 v[18:19], v[18:19], v[58:59]
	v_pk_add_f32 v[20:21], v[20:21], v[60:61]
	v_pk_add_f32 v[18:19], v[18:19], v[78:79] op_sel_hi:[1,0]
	v_pk_add_f32 v[20:21], v[20:21], v[78:79] op_sel_hi:[1,0]
	v_pk_fma_f32 v[18:19], v[72:73], v[76:77], v[18:19] op_sel:[0,1,0] op_sel_hi:[1,1,1]
	v_pk_fma_f32 v[20:21], v[74:75], v[76:77], v[20:21] op_sel:[0,1,0] op_sel_hi:[1,1,1]
	v_pk_add_f32 v[34:35], v[34:35], v[18:19]
	v_pk_fma_f32 v[36:37], v[18:19], v[18:19], v[36:37]
	v_pk_add_f32 v[34:35], v[34:35], v[20:21]
	v_pk_fma_f32 v[36:37], v[20:21], v[20:21], v[36:37]
	ds_read2st64_b32 v[50:51], v221 offset0:36 offset1:37
	ds_read2st64_b32 v[52:53], v221 offset0:38 offset1:39
	ds_read2st64_b32 v[62:63], v67 offset0:144 offset1:146
	ds_read2st64_b32 v[64:65], v67 offset0:148 offset1:150
	s_waitcnt lgkmcnt(0)
	v_pk_add_f32 v[22:23], v[22:23], v[50:51]
	v_pk_add_f32 v[24:25], v[24:25], v[52:53]
	v_pk_add_f32 v[22:23], v[22:23], v[78:79] op_sel_hi:[1,0]
	v_pk_add_f32 v[24:25], v[24:25], v[78:79] op_sel_hi:[1,0]
	v_pk_fma_f32 v[22:23], v[62:63], v[76:77], v[22:23] op_sel:[0,1,0] op_sel_hi:[1,1,1]
	v_pk_fma_f32 v[24:25], v[64:65], v[76:77], v[24:25] op_sel:[0,1,0] op_sel_hi:[1,1,1]
	v_pk_add_f32 v[34:35], v[34:35], v[22:23]
	v_pk_fma_f32 v[36:37], v[22:23], v[22:23], v[36:37]
	v_pk_add_f32 v[34:35], v[34:35], v[24:25]
	v_pk_fma_f32 v[36:37], v[24:25], v[24:25], v[36:37]
	s_mov_b64 s[40:41], exec
	s_and_b64 exec, exec, s[0:1]
	ds_read2st64_b32 v[50:51], v221 offset0:40 offset1:41
	ds_read2st64_b32 v[52:53], v221 offset0:42 offset1:43
	ds_read2st64_b32 v[62:63], v67 offset0:160 offset1:162
	ds_read2st64_b32 v[64:65], v67 offset0:164 offset1:166
	s_waitcnt lgkmcnt(0)
	v_pk_add_f32 v[26:27], v[26:27], v[50:51]
	v_pk_add_f32 v[28:29], v[28:29], v[52:53]
	v_pk_add_f32 v[26:27], v[26:27], v[78:79] op_sel_hi:[1,0]
	v_pk_add_f32 v[28:29], v[28:29], v[78:79] op_sel_hi:[1,0]
	v_pk_fma_f32 v[26:27], v[62:63], v[76:77], v[26:27] op_sel:[0,1,0] op_sel_hi:[1,1,1]
	v_pk_fma_f32 v[28:29], v[64:65], v[76:77], v[28:29] op_sel:[0,1,0] op_sel_hi:[1,1,1]
	v_pk_add_f32 v[34:35], v[34:35], v[26:27]
	v_pk_fma_f32 v[36:37], v[26:27], v[26:27], v[36:37]
	v_pk_add_f32 v[34:35], v[34:35], v[28:29]
	v_pk_fma_f32 v[36:37], v[28:29], v[28:29], v[36:37]
	s_mov_b64 exec, s[40:41]
	v_add_f32_e32 v34, v34, v35
	v_add_f32_e32 v36, v36, v37
	v_mov_b32_e32 v35, v34
	v_mov_b32_e32 v37, v36
	s_nop 1
	v_permlane32_swap_b32_e32 v34, v35
	v_permlane32_swap_b32_e32 v36, v37
	v_add_f32_e32 v34, v34, v35
	v_add_f32_e32 v36, v36, v37
	v_cndmask_b32_e64 v38, v36, v34, s[0:1]
	ds_write_b32 v236, v38
